# GU L0-L2 epilogues: the four row-step table LDS reads issued together after the first one (spare VGPRs v216-221), one exposed LDS round trip per unit instead of four
# speedup vs baseline: 1.0036x; 1.0026x over previous
; __device__ __forceinline__ float fast_sigmoid(float x) { return __builtin_amdgcn_rcpf(1.0f + __expf(-x)); }
;     __device__ __forceinline__ void operator()(const f32x4 (&acc)[2][2][4][2], const Unit& u, int wr, int wc, int fr, int fq) const {
;         const int row0 = u.pm * BM + wr * 64 + fr, col0 = u.pn * HALF + wc * 32 + 8 * fq; const int sl = IN8 ? rt.slot(u.pm) : 0;
;         f32x4 cg[2], cu[2];
; #pragma unroll
;         for (int n = 0; n < 2; ++n) { cg[n] = IN8 ? *(const f32x4*)(cstep + u.pn * BM + wc * 32 + 8 * fq + 4 * n) : (f32x4){1.f, 1.f, 1.f, 1.f}; cu[n] = IN8 ? *(const f32x4*)(cstep + u.pn * BM + HALF + wc * 32 + 8 * fq + 4 * n) : (f32x4){1.f, 1.f, 1.f, 1.f}; }
; #pragma unroll
;         for (int ai = 0; ai < 2; ++ai)
; #pragma unroll
;             for (int m = 0; m < 4; ++m) { const size_t off = (size_t)(row0 + ai * HALF + m * 16) * ldc + col0;
;                 const float rs = IN8 ? rt.tab[sl * 256 + wr * 64 + ai * HALF + m * 16 + fr] : isc;
;                 const float rsn = rs * -1.4426950408889634f, rs2 = rs * rs; (void)rsn; (void)rs2;
;                 float o[8];
; #pragma unroll
;                 for (int n = 0; n < 2; ++n)
; #pragma unroll
;                     for (int e = 0; e < 4; ++e) { const float ga = acc[ai][0][m][n][e], ua = acc[ai][1][m][n][e];
;                         if (IN8) {
;                             const float gq = (float)__float_as_int(ga) * cg[n][e], uq = (float)__float_as_int(ua) * cu[n][e];
;                             const float sg = __builtin_amdgcn_rcpf(1.0f + __builtin_amdgcn_exp2f(gq * rsn));
;                             o[4 * n + e] = (gq * uq) * (sg * rs2); }
;                         else { const float g = ga * rs, up = ua * rs; o[4 * n + e] = g * fast_sigmoid(g) * up; } }
;                 if (F8) { unsigned w0 = 0u, w1 = 0u;
; #pragma unroll
;                     for (int e = 0; e < 8; ++e) o[e] = __builtin_amdgcn_fmed3f(o[e] * H8_SCALE, -448.0f, 448.0f);
;                     w0 = __builtin_amdgcn_cvt_pk_fp8_f32(o[0], o[1], w0, false); w0 = __builtin_amdgcn_cvt_pk_fp8_f32(o[2], o[3], w0, true);
;                     w1 = __builtin_amdgcn_cvt_pk_fp8_f32(o[4], o[5], w1, false); w1 = __builtin_amdgcn_cvt_pk_fp8_f32(o[6], o[7], w1, true);
;                     typedef unsigned u32x2_ __attribute__((ext_vector_type(2))); *(u32x2_*)((unsigned char*)O + off) = (u32x2_){w0, w1}; }
.LBB0_230:
	s_lshl_b32 s24, s63, 8
	s_ashr_i32 s25, s24, 31
	s_nop 0
	v_mov_b32_e32 v142, v226
	v_mov_b32_e32 v143, v227
	v_mov_b32_e32 v144, v228
	v_mov_b32_e32 v145, v229
	v_mov_b32_e32 v138, v230
	v_mov_b32_e32 v139, v231
	v_mov_b32_e32 v140, v232
	v_mov_b32_e32 v141, v233
	v_mov_b32_e32 v134, v234
	v_mov_b32_e32 v135, v235
	v_mov_b32_e32 v136, v236
	v_mov_b32_e32 v137, v237
	s_nop 0
	v_mov_b32_e32 v130, v238
	v_mov_b32_e32 v131, v239
	v_mov_b32_e32 v132, v240
	v_mov_b32_e32 v133, v241
	s_add_i32 s15, s34, 0x20204
	v_cvt_f32_i32_e32 v172, v118
	v_mov_b32_e32 v118, s15
	v_cvt_f32_i32_e32 v173, v119
	ds_read2_b32 v[118:119], v118 offset1:1
	s_add_i32 s17, s34, 0x2020c
	s_add_i32 s24, s34, 0x20214
	s_add_i32 s25, s34, 0x2021c
	v_mov_b32_e32 v169, s17
	v_mov_b32_e32 v171, s24
	v_mov_b32_e32 v178, s25
	ds_read2_b32 v[174:175], v169 offset1:1
	ds_read2_b32 v[176:177], v171 offset1:1
	ds_read_b32 v169, v178
	s_waitcnt lgkmcnt(0)
	v_cmp_eq_u32_e32 vcc, s22, v118
	v_cvt_f32_i32_e32 v127, v127
	v_cvt_f32_i32_e32 v126, v126
	v_cndmask_b32_e64 v118, 0, 1, vcc
	v_cmp_ne_u32_e32 vcc, s22, v119
	v_cvt_f32_i32_e32 v123, v123
	v_cvt_f32_i32_e32 v122, v122
	v_cndmask_b32_e32 v118, 2, v118, vcc
	v_cmp_ne_u32_e32 vcc, s22, v174
	v_cvt_f32_i32_e32 v129, v129
	v_cvt_f32_i32_e32 v128, v128
	v_cndmask_b32_e32 v118, 3, v118, vcc
	v_cmp_ne_u32_e32 vcc, s22, v175
	v_cvt_f32_i32_e32 v125, v125
	v_cvt_f32_i32_e32 v124, v124
	v_cndmask_b32_e32 v118, 4, v118, vcc
	v_cmp_ne_u32_e32 vcc, s22, v176
	v_cvt_f32_i32_e32 v121, v121
	v_cvt_f32_i32_e32 v120, v120
	v_cndmask_b32_e32 v118, 5, v118, vcc
	v_cmp_ne_u32_e32 vcc, s22, v177
	v_cvt_f32_i32_e32 v115, v115
	v_cvt_f32_i32_e32 v114, v114
	v_cndmask_b32_e32 v118, 6, v118, vcc
	v_cmp_ne_u32_e32 vcc, s22, v169
	v_cvt_f32_i32_e32 v117, v117
	v_cvt_f32_i32_e32 v116, v116
	v_cndmask_b32_e32 v118, 7, v118, vcc
	v_lshl_or_b32 v170, s63, 7, v165
	v_readfirstlane_b32 s15, v118
	v_lshl_add_u32 v168, s22, 8, v1
	v_ashrrev_i32_e32 v171, 31, v170
	v_lshl_add_u32 v118, s15, 10, v166
	ds_read2_b32 v[174:175], v118 offset1:16
	ds_read2_b32 v[216:217], v118 offset0:32 offset1:48
	ds_read2_b32 v[218:219], v118 offset0:128 offset1:144
	ds_read2_b32 v[220:221], v118 offset0:160 offset1:176
	v_cvt_f32_i32_e32 v113, v113
	v_cvt_f32_i32_e32 v112, v112
	v_cvt_f32_i32_e32 v107, v107
	v_cvt_f32_i32_e32 v106, v106
	s_waitcnt lgkmcnt(0)
	v_mul_f32_e32 v119, 0xbfb8aa3b, v174
	v_mul_f32_e32 v174, v174, v174
	v_cvt_f32_i32_e32 v109, v109
	v_cvt_f32_i32_e32 v108, v108
	v_cvt_f32_i32_e32 v103, v103
	v_cvt_f32_i32_e32 v102, v102
	v_cvt_f32_i32_e32 v99, v99
	v_cvt_f32_i32_e32 v98, v98
	v_cvt_f32_i32_e32 v105, v105
	v_cvt_f32_i32_e32 v104, v104
	v_cvt_f32_i32_e32 v101, v101
	v_cvt_f32_i32_e32 v100, v100
	v_cvt_f32_i32_e32 v95, v95
	v_cvt_f32_i32_e32 v94, v94
	v_cvt_f32_i32_e32 v91, v91
	v_cvt_f32_i32_e32 v90, v90
	v_cvt_f32_i32_e32 v97, v97
	v_cvt_f32_i32_e32 v96, v96
	v_cvt_f32_i32_e32 v93, v93
	v_cvt_f32_i32_e32 v92, v92
	v_cvt_f32_i32_e32 v87, v87
	v_cvt_f32_i32_e32 v86, v86
	v_cvt_f32_i32_e32 v83, v83
	v_cvt_f32_i32_e32 v82, v82
	v_cvt_f32_i32_e32 v89, v89
	v_cvt_f32_i32_e32 v88, v88
	s_nop 0
	v_pk_mul_f32 v[126:127], v[142:143], v[126:127]
	v_pk_mul_f32 v[122:123], v[138:139], v[122:123]
	v_pk_mul_f32 v[128:129], v[144:145], v[128:129]
	v_pk_mul_f32 v[124:125], v[140:141], v[124:125]
	v_pk_mul_f32 v[172:173], v[134:135], v[172:173]
	v_pk_mul_f32 v[176:177], v[136:137], v[120:121]
	v_mul_f32_e32 v169, v126, v119
	v_mul_f32_e32 v178, v127, v119
	v_pk_mul_f32 v[120:121], v[126:127], v[122:123]
	v_mul_f32_e32 v126, v128, v119
	v_mul_f32_e32 v127, v129, v119
	v_pk_mul_f32 v[122:123], v[128:129], v[124:125]
	v_mul_f32_e32 v124, v172, v119
	v_mul_f32_e32 v125, v173, v119
	v_exp_f32_e32 v129, v169
	v_exp_f32_e32 v169, v178
	v_exp_f32_e32 v126, v126
	v_exp_f32_e32 v127, v127
	v_exp_f32_e32 v124, v124
	v_exp_f32_e32 v125, v125
	v_pk_mul_f32 v[114:115], v[130:131], v[114:115]
	v_mul_f32_e32 v128, v176, v119
	v_pk_mul_f32 v[114:115], v[172:173], v[114:115]
	v_exp_f32_e32 v172, v128
	v_add_f32_e32 v128, 1.0, v129
	v_add_f32_e32 v129, 1.0, v169
	v_add_f32_e32 v126, 1.0, v126
	v_add_f32_e32 v127, 1.0, v127
	v_add_f32_e32 v169, 1.0, v124
	v_add_f32_e32 v173, 1.0, v125
	v_rcp_f32_e32 v124, v128
	v_rcp_f32_e32 v125, v129
	v_rcp_f32_e32 v126, v126
	v_rcp_f32_e32 v127, v127
	v_rcp_f32_e32 v128, v169
	v_rcp_f32_e32 v129, v173
	v_mul_f32_e32 v119, v177, v119
	v_exp_f32_e32 v119, v119
	v_pk_mul_f32 v[124:125], v[174:175], v[124:125] op_sel_hi:[0,1]
	v_pk_mul_f32 v[126:127], v[174:175], v[126:127] op_sel_hi:[0,1]
	v_pk_mul_f32 v[120:121], v[120:121], v[124:125]
	v_pk_mul_f32 v[122:123], v[122:123], v[126:127]
	v_cvt_pk_bf16_f32 v120, v120, v121
	v_cvt_pk_bf16_f32 v121, v122, v123
	v_pk_mul_f32 v[122:123], v[174:175], v[128:129] op_sel_hi:[0,1]
	v_pk_mul_f32 v[114:115], v[114:115], v[122:123]
	v_add_f32_e32 v122, 1.0, v172
	v_add_f32_e32 v119, 1.0, v119
	v_rcp_f32_e32 v124, v122
	v_rcp_f32_e32 v125, v119
	v_cvt_pk_bf16_f32 v122, v114, v115
	v_pk_mul_f32 v[114:115], v[132:133], v[116:117]
	v_mul_f32_e32 v119, 0xbfb8aa3b, v175
	v_pk_mul_f32 v[114:115], v[176:177], v[114:115]
	v_pk_mul_f32 v[116:117], v[174:175], v[124:125] op_sel_hi:[0,1]
	v_cvt_f32_i32_e32 v125, v111
	v_cvt_f32_i32_e32 v124, v110
	v_pk_mul_f32 v[114:115], v[114:115], v[116:117]
	v_lshlrev_b64 v[110:111], 1, v[170:171]
	v_cvt_pk_bf16_f32 v123, v114, v115
	v_mov_b64_e32 v[114:115], s[6:7]
	v_mad_i64_i32 v[116:117], s[24:25], v168, s62, v[114:115]
	v_lshl_add_u64 v[116:117], v[116:117], 0, v[110:111]
	v_pk_mul_f32 v[124:125], v[142:143], v[124:125]
	global_store_dwordx4 v[116:117], v[120:123], off nt
; __device__ __forceinline__ float fast_sigmoid(float x) { return __builtin_amdgcn_rcpf(1.0f + __expf(-x)); }
;     __device__ __forceinline__ void operator()(const f32x4 (&acc)[2][2][4][2], const Unit& u, int wr, int wc, int fr, int fq) const {
;     ...
;             for (int m = 0; m < 4; ++m) { const size_t off = (size_t)(row0 + ai * HALF + m * 16) * ldc + col0;
;                 const float rs = IN8 ? rt.tab[sl * 256 + wr * 64 + ai * HALF + m * 16 + fr] : isc;
;                 const float rsn = rs * -1.4426950408889634f, rs2 = rs * rs; (void)rsn; (void)rs2;
;                 float o[8];
; #pragma unroll
;                 for (int n = 0; n < 2; ++n)
; #pragma unroll
;                     for (int e = 0; e < 4; ++e) { const float ga = acc[ai][0][m][n][e], ua = acc[ai][1][m][n][e];
;                         if (IN8) {
;                             const float gq = (float)__float_as_int(ga) * cg[n][e], uq = (float)__float_as_int(ua) * cu[n][e];
;                             const float sg = __builtin_amdgcn_rcpf(1.0f + __builtin_amdgcn_exp2f(gq * rsn));
;                             o[4 * n + e] = (gq * uq) * (sg * rs2); }
;                         else { const float g = ga * rs, up = ua * rs; o[4 * n + e] = g * fast_sigmoid(g) * up; } }
;                 if (F8) { unsigned w0 = 0u, w1 = 0u;
; #pragma unroll
;                     for (int e = 0; e < 8; ++e) o[e] = __builtin_amdgcn_fmed3f(o[e] * H8_SCALE, -448.0f, 448.0f);
;                     w0 = __builtin_amdgcn_cvt_pk_fp8_f32(o[0], o[1], w0, false); w0 = __builtin_amdgcn_cvt_pk_fp8_f32(o[2], o[3], w0, true);
;                     w1 = __builtin_amdgcn_cvt_pk_fp8_f32(o[4], o[5], w1, false); w1 = __builtin_amdgcn_cvt_pk_fp8_f32(o[6], o[7], w1, true);
;                     typedef unsigned u32x2_ __attribute__((ext_vector_type(2))); *(u32x2_*)((unsigned char*)O + off) = (u32x2_){w0, w1}; }
;                 else { u32x4 w; w.x = cvt_pk_bf16(o[0], o[1]); w.y = cvt_pk_bf16(o[2], o[3]); w.z = cvt_pk_bf16(o[4], o[5]); w.w = cvt_pk_bf16(o[6], o[7]);
;                     __builtin_nontemporal_store(w, (u32x4*)((bf16_t*)O + off)); } }
	v_mul_f32_e32 v126, v124, v119
	v_exp_f32_e32 v126, v126
	v_mul_f32_e32 v121, v125, v119
	v_exp_f32_e32 v121, v121
	v_pk_mul_f32 v[112:113], v[144:145], v[112:113]
	v_add_f32_e32 v120, 1.0, v126
	v_rcp_f32_e32 v120, v120
	v_add_f32_e32 v121, 1.0, v121
	v_rcp_f32_e32 v121, v121
	v_mul_f32_e32 v122, v112, v119
	v_exp_f32_e32 v122, v122
	v_or_b32_e32 v117, 16, v168
	v_mul_f32_e32 v116, v175, v175
	v_pk_mul_f32 v[106:107], v[138:139], v[106:107]
	v_pk_mul_f32 v[120:121], v[116:117], v[120:121] op_sel_hi:[0,1]
	v_pk_mul_f32 v[106:107], v[124:125], v[106:107]
	v_pk_mul_f32 v[108:109], v[140:141], v[108:109]
	v_pk_mul_f32 v[106:107], v[106:107], v[120:121]
	v_pk_mul_f32 v[108:109], v[112:113], v[108:109]
	v_cvt_pk_bf16_f32 v106, v106, v107
	v_add_f32_e32 v107, 1.0, v122
	v_rcp_f32_e32 v120, v107
	v_mul_f32_e32 v107, v113, v119
	v_exp_f32_e32 v107, v107
	v_pk_mul_f32 v[102:103], v[134:135], v[102:103]
	v_pk_mul_f32 v[98:99], v[130:131], v[98:99]
	v_pk_mul_f32 v[104:105], v[136:137], v[104:105]
	v_add_f32_e32 v107, 1.0, v107
	v_rcp_f32_e32 v121, v107
	v_mul_f32_e32 v107, v102, v119
	v_exp_f32_e32 v122, v107
	v_pk_mul_f32 v[98:99], v[102:103], v[98:99]
	v_pk_mul_f32 v[112:113], v[116:117], v[120:121] op_sel_hi:[0,1]
	v_pk_mul_f32 v[108:109], v[108:109], v[112:113]
	v_mul_f32_e32 v112, v104, v119
	v_cvt_pk_bf16_f32 v107, v108, v109
	v_mul_f32_e32 v109, v103, v119
	v_exp_f32_e32 v109, v109
	v_add_f32_e32 v108, 1.0, v122
	v_rcp_f32_e32 v108, v108
	v_exp_f32_e32 v112, v112
	v_add_f32_e32 v109, 1.0, v109
	v_rcp_f32_e32 v109, v109
	v_pk_mul_f32 v[94:95], v[142:143], v[94:95]
	v_pk_mul_f32 v[90:91], v[138:139], v[90:91]
	v_pk_mul_f32 v[92:93], v[140:141], v[92:93]
	v_pk_mul_f32 v[102:103], v[116:117], v[108:109] op_sel_hi:[0,1]
	v_pk_mul_f32 v[98:99], v[98:99], v[102:103]
	v_mul_f32_e32 v103, v105, v119
	v_exp_f32_e32 v103, v103
	v_add_f32_e32 v102, 1.0, v112
	v_rcp_f32_e32 v102, v102
	v_cvt_pk_bf16_f32 v108, v98, v99
	v_add_f32_e32 v103, 1.0, v103
	v_rcp_f32_e32 v103, v103
	v_pk_mul_f32 v[98:99], v[132:133], v[100:101]
	v_pk_mul_f32 v[90:91], v[94:95], v[90:91]
	v_pk_mul_f32 v[98:99], v[104:105], v[98:99]
	v_pk_mul_f32 v[100:101], v[116:117], v[102:103] op_sel_hi:[0,1]
	v_pk_mul_f32 v[98:99], v[98:99], v[100:101]
	v_mad_i64_i32 v[100:101], s[24:25], v117, s62, v[114:115]
	v_cvt_pk_bf16_f32 v109, v98, v99
	s_nop 0
	v_lshl_add_u64 v[100:101], v[100:101], 0, v[110:111]
	global_store_dwordx4 v[100:101], v[106:109], off nt
	v_pk_mul_f32 v[86:87], v[134:135], v[86:87]
	v_pk_mul_f32 v[82:83], v[130:131], v[82:83]
	s_waitcnt lgkmcnt(0)
	v_mul_f32_e32 v102, 0xbfb8aa3b, v216
	v_mul_f32_e32 v103, v94, v102
	v_mul_f32_e32 v101, v95, v102
	v_exp_f32_e32 v103, v103
	v_exp_f32_e32 v101, v101
	v_pk_mul_f32 v[94:95], v[144:145], v[96:97]
	v_mul_f32_e32 v216, v216, v216
	v_add_f32_e32 v100, 1.0, v103
	v_add_f32_e32 v101, 1.0, v101
	v_rcp_f32_e32 v100, v100
	v_rcp_f32_e32 v101, v101
	v_mul_f32_e32 v96, v94, v102
	v_exp_f32_e32 v103, v96
	v_pk_mul_f32 v[92:93], v[94:95], v[92:93]
	v_pk_mul_f32 v[96:97], v[216:217], v[100:101] op_sel_hi:[0,1]
	v_pk_mul_f32 v[90:91], v[90:91], v[96:97]
	v_pk_mul_f32 v[88:89], v[136:137], v[88:89]
	v_cvt_pk_bf16_f32 v90, v90, v91
	v_add_f32_e32 v91, 1.0, v103
	v_rcp_f32_e32 v96, v91
	v_mul_f32_e32 v91, v95, v102
	v_exp_f32_e32 v91, v91
	v_pk_mul_f32 v[82:83], v[86:87], v[82:83]
	v_cvt_f32_i32_e32 v85, v85
	v_cvt_f32_i32_e32 v84, v84
	v_add_f32_e32 v91, 1.0, v91
	v_rcp_f32_e32 v97, v91
	v_mul_f32_e32 v91, v86, v102
	v_exp_f32_e32 v100, v91
	v_cvt_f32_i32_e32 v79, v79
	v_pk_mul_f32 v[94:95], v[216:217], v[96:97] op_sel_hi:[0,1]
	v_pk_mul_f32 v[92:93], v[92:93], v[94:95]
	v_mul_f32_e32 v94, v88, v102
	v_cvt_pk_bf16_f32 v91, v92, v93
	v_mul_f32_e32 v93, v87, v102
	v_exp_f32_e32 v93, v93
	v_add_f32_e32 v92, 1.0, v100
	v_rcp_f32_e32 v92, v92
	v_exp_f32_e32 v94, v94
	v_add_f32_e32 v93, 1.0, v93
	v_rcp_f32_e32 v93, v93
	v_cvt_f32_i32_e32 v78, v78
	v_cvt_f32_i32_e32 v75, v75
	v_cvt_f32_i32_e32 v74, v74
	v_pk_mul_f32 v[86:87], v[216:217], v[92:93] op_sel_hi:[0,1]
	v_pk_mul_f32 v[82:83], v[82:83], v[86:87]
	v_mul_f32_e32 v87, v89, v102
	v_exp_f32_e32 v87, v87
	v_add_f32_e32 v86, 1.0, v94
	v_rcp_f32_e32 v86, v86
	v_cvt_pk_bf16_f32 v92, v82, v83
	v_add_f32_e32 v87, 1.0, v87
	v_rcp_f32_e32 v87, v87
	v_pk_mul_f32 v[82:83], v[132:133], v[84:85]
	v_pk_mul_f32 v[78:79], v[142:143], v[78:79]
	v_pk_mul_f32 v[82:83], v[88:89], v[82:83]
	v_pk_mul_f32 v[84:85], v[216:217], v[86:87] op_sel_hi:[0,1]
	v_mul_f32_e32 v86, 0xbfb8aa3b, v217
	v_pk_mul_f32 v[82:83], v[82:83], v[84:85]
	v_mul_f32_e32 v84, v78, v86
	v_mul_f32_e32 v85, v79, v86
	v_exp_f32_e32 v84, v84
	v_exp_f32_e32 v85, v85
	v_cvt_f32_i32_e32 v81, v81
	v_cvt_f32_i32_e32 v80, v80
	v_add_f32_e32 v84, 1.0, v84
	v_pk_mul_f32 v[74:75], v[138:139], v[74:75]
	v_add_f32_e32 v85, 1.0, v85
	v_or_b32_e32 v104, 32, v168
	v_rcp_f32_e32 v84, v84
	v_rcp_f32_e32 v85, v85
	v_pk_mul_f32 v[74:75], v[78:79], v[74:75]
	v_pk_mul_f32 v[78:79], v[144:145], v[80:81]
	v_cvt_pk_bf16_f32 v93, v82, v83
	v_mad_i64_i32 v[82:83], s[24:25], v104, s62, v[114:115]
	v_mul_f32_e32 v80, v78, v86
	v_lshl_add_u64 v[82:83], v[82:83], 0, v[110:111]
	v_exp_f32_e32 v87, v80
	global_store_dwordx4 v[82:83], v[90:93], off nt
	v_or_b32_e32 v83, 48, v168
	v_mul_f32_e32 v82, v217, v217
	v_pk_mul_f32 v[80:81], v[82:83], v[84:85] op_sel_hi:[0,1]
	v_pk_mul_f32 v[74:75], v[74:75], v[80:81]
	v_cvt_f32_i32_e32 v77, v77
	v_cvt_pk_bf16_f32 v74, v74, v75
	v_add_f32_e32 v75, 1.0, v87
	v_rcp_f32_e32 v80, v75
	v_mul_f32_e32 v75, v79, v86
	v_exp_f32_e32 v75, v75
	v_cvt_f32_i32_e32 v76, v76
	v_cvt_f32_i32_e32 v71, v71
	v_cvt_f32_i32_e32 v70, v70
	v_add_f32_e32 v75, 1.0, v75
; __device__ __forceinline__ float fast_sigmoid(float x) { return __builtin_amdgcn_rcpf(1.0f + __expf(-x)); }
;     __device__ __forceinline__ void operator()(const f32x4 (&acc)[2][2][4][2], const Unit& u, int wr, int wc, int fr, int fq) const {
;     ...
;             for (int m = 0; m < 4; ++m) { const size_t off = (size_t)(row0 + ai * HALF + m * 16) * ldc + col0;
;                 const float rs = IN8 ? rt.tab[sl * 256 + wr * 64 + ai * HALF + m * 16 + fr] : isc;
;                 const float rsn = rs * -1.4426950408889634f, rs2 = rs * rs; (void)rsn; (void)rs2;
;                 float o[8];
; #pragma unroll
;                 for (int n = 0; n < 2; ++n)
; #pragma unroll
;                     for (int e = 0; e < 4; ++e) { const float ga = acc[ai][0][m][n][e], ua = acc[ai][1][m][n][e];
;                         if (IN8) {
;                             const float gq = (float)__float_as_int(ga) * cg[n][e], uq = (float)__float_as_int(ua) * cu[n][e];
;                             const float sg = __builtin_amdgcn_rcpf(1.0f + __builtin_amdgcn_exp2f(gq * rsn));
;                             o[4 * n + e] = (gq * uq) * (sg * rs2); }
;                         else { const float g = ga * rs, up = ua * rs; o[4 * n + e] = g * fast_sigmoid(g) * up; } }
;                 if (F8) { unsigned w0 = 0u, w1 = 0u;
; #pragma unroll
;                     for (int e = 0; e < 8; ++e) o[e] = __builtin_amdgcn_fmed3f(o[e] * H8_SCALE, -448.0f, 448.0f);
;                     w0 = __builtin_amdgcn_cvt_pk_fp8_f32(o[0], o[1], w0, false); w0 = __builtin_amdgcn_cvt_pk_fp8_f32(o[2], o[3], w0, true);
;                     w1 = __builtin_amdgcn_cvt_pk_fp8_f32(o[4], o[5], w1, false); w1 = __builtin_amdgcn_cvt_pk_fp8_f32(o[6], o[7], w1, true);
;                     typedef unsigned u32x2_ __attribute__((ext_vector_type(2))); *(u32x2_*)((unsigned char*)O + off) = (u32x2_){w0, w1}; }
;                 else { u32x4 w; w.x = cvt_pk_bf16(o[0], o[1]); w.y = cvt_pk_bf16(o[2], o[3]); w.z = cvt_pk_bf16(o[4], o[5]); w.w = cvt_pk_bf16(o[6], o[7]);
;                     __builtin_nontemporal_store(w, (u32x4*)((bf16_t*)O + off)); } }
	v_rcp_f32_e32 v81, v75
	v_pk_mul_f32 v[76:77], v[140:141], v[76:77]
	v_pk_mul_f32 v[70:71], v[134:135], v[70:71]
	v_pk_mul_f32 v[76:77], v[78:79], v[76:77]
	v_pk_mul_f32 v[78:79], v[82:83], v[80:81] op_sel_hi:[0,1]
	v_mul_f32_e32 v75, v70, v86
	v_pk_mul_f32 v[76:77], v[76:77], v[78:79]
	v_exp_f32_e32 v84, v75
	v_cvt_pk_bf16_f32 v75, v76, v77
	v_mul_f32_e32 v77, v71, v86
	v_exp_f32_e32 v77, v77
	v_add_f32_e32 v76, 1.0, v84
	v_cvt_f32_i32_e32 v67, v67
	v_cvt_f32_i32_e32 v66, v66
	v_add_f32_e32 v77, 1.0, v77
	v_rcp_f32_e32 v76, v76
	v_cvt_f32_i32_e32 v73, v73
	v_cvt_f32_i32_e32 v72, v72
	v_rcp_f32_e32 v77, v77
	v_pk_mul_f32 v[66:67], v[130:131], v[66:67]
	v_cvt_f32_i32_e32 v69, v69
	v_pk_mul_f32 v[72:73], v[136:137], v[72:73]
	v_pk_mul_f32 v[66:67], v[70:71], v[66:67]
	v_pk_mul_f32 v[70:71], v[82:83], v[76:77] op_sel_hi:[0,1]
	v_mul_f32_e32 v78, v72, v86
	v_pk_mul_f32 v[66:67], v[66:67], v[70:71]
	v_mul_f32_e32 v71, v73, v86
	v_exp_f32_e32 v78, v78
	v_exp_f32_e32 v71, v71
	v_cvt_f32_i32_e32 v68, v68
	v_cvt_pk_bf16_f32 v76, v66, v67
	v_add_f32_e32 v70, 1.0, v78
	v_add_f32_e32 v71, 1.0, v71
	v_rcp_f32_e32 v70, v70
	v_rcp_f32_e32 v71, v71
	v_pk_mul_f32 v[66:67], v[132:133], v[68:69]
	v_cvt_f32_i32_e32 v63, v63
	v_pk_mul_f32 v[66:67], v[72:73], v[66:67]
	v_pk_mul_f32 v[68:69], v[82:83], v[70:71] op_sel_hi:[0,1]
	v_pk_mul_f32 v[66:67], v[66:67], v[68:69]
	v_cvt_f32_i32_e32 v62, v62
	v_cvt_pk_bf16_f32 v77, v66, v67
	s_nop 0
	v_mad_i64_i32 v[68:69], s[24:25], v83, s62, v[114:115]
	v_lshl_add_u64 v[68:69], v[68:69], 0, v[110:111]
	v_pk_mul_f32 v[62:63], v[142:143], v[62:63]
	s_waitcnt lgkmcnt(0)
	v_mul_f32_e32 v70, 0xbfb8aa3b, v218
	v_mul_f32_e32 v71, v62, v70
	global_store_dwordx4 v[68:69], v[74:77], off nt
	v_mul_f32_e32 v69, v63, v70
	v_exp_f32_e32 v71, v71
	v_cvt_f32_i32_e32 v59, v59
	v_cvt_f32_i32_e32 v58, v58
	v_exp_f32_e32 v69, v69
	v_cvt_f32_i32_e32 v65, v65
	v_cvt_f32_i32_e32 v64, v64
	v_add_f32_e32 v68, 1.0, v71
	v_pk_mul_f32 v[58:59], v[138:139], v[58:59]
	v_add_f32_e32 v69, 1.0, v69
	v_rcp_f32_e32 v68, v68
	v_rcp_f32_e32 v69, v69
	v_pk_mul_f32 v[58:59], v[62:63], v[58:59]
	v_pk_mul_f32 v[62:63], v[144:145], v[64:65]
	v_mul_f32_e32 v218, v218, v218
	v_mul_f32_e32 v64, v62, v70
	v_exp_f32_e32 v71, v64
	v_pk_mul_f32 v[64:65], v[218:219], v[68:69] op_sel_hi:[0,1]
	v_pk_mul_f32 v[58:59], v[58:59], v[64:65]
	v_cvt_f32_i32_e32 v61, v61
	v_cvt_pk_bf16_f32 v58, v58, v59
	v_add_f32_e32 v59, 1.0, v71
	v_rcp_f32_e32 v64, v59
	v_mul_f32_e32 v59, v63, v70
	v_exp_f32_e32 v59, v59
	v_cvt_f32_i32_e32 v60, v60
	v_cvt_f32_i32_e32 v55, v55
	v_cvt_f32_i32_e32 v54, v54
	v_add_f32_e32 v59, 1.0, v59
	v_rcp_f32_e32 v65, v59
	v_pk_mul_f32 v[60:61], v[140:141], v[60:61]
	v_pk_mul_f32 v[54:55], v[134:135], v[54:55]
	v_pk_mul_f32 v[60:61], v[62:63], v[60:61]
	v_pk_mul_f32 v[62:63], v[218:219], v[64:65] op_sel_hi:[0,1]
	v_mul_f32_e32 v59, v54, v70
	v_pk_mul_f32 v[60:61], v[60:61], v[62:63]
	v_exp_f32_e32 v68, v59
	v_cvt_pk_bf16_f32 v59, v60, v61
	v_mul_f32_e32 v61, v55, v70
	v_exp_f32_e32 v61, v61
	v_add_f32_e32 v60, 1.0, v68
	v_cvt_f32_i32_e32 v51, v51
	v_cvt_f32_i32_e32 v50, v50
	v_add_f32_e32 v61, 1.0, v61
	v_rcp_f32_e32 v60, v60
	v_cvt_f32_i32_e32 v57, v57
	v_cvt_f32_i32_e32 v56, v56
	v_rcp_f32_e32 v61, v61
	v_pk_mul_f32 v[50:51], v[130:131], v[50:51]
	v_cvt_f32_i32_e32 v53, v53
	v_pk_mul_f32 v[56:57], v[136:137], v[56:57]
	v_pk_mul_f32 v[50:51], v[54:55], v[50:51]
	v_pk_mul_f32 v[54:55], v[218:219], v[60:61] op_sel_hi:[0,1]
	v_mul_f32_e32 v62, v56, v70
	v_pk_mul_f32 v[50:51], v[50:51], v[54:55]
	v_mul_f32_e32 v55, v57, v70
	v_exp_f32_e32 v62, v62
	v_exp_f32_e32 v55, v55
	v_cvt_f32_i32_e32 v52, v52
	v_cvt_f32_i32_e32 v47, v47
	v_add_f32_e32 v54, 1.0, v62
	v_add_f32_e32 v55, 1.0, v55
	v_rcp_f32_e32 v54, v54
	v_rcp_f32_e32 v55, v55
	v_cvt_f32_i32_e32 v46, v46
	v_cvt_pk_bf16_f32 v60, v50, v51
	v_pk_mul_f32 v[50:51], v[132:133], v[52:53]
	v_pk_mul_f32 v[52:53], v[218:219], v[54:55] op_sel_hi:[0,1]
	v_pk_mul_f32 v[50:51], v[56:57], v[50:51]
	v_mul_f32_e32 v54, 0xbfb8aa3b, v219
	v_pk_mul_f32 v[46:47], v[142:143], v[46:47]
	v_pk_mul_f32 v[50:51], v[50:51], v[52:53]
	v_mul_f32_e32 v52, v46, v54
	v_mul_f32_e32 v53, v47, v54
	v_exp_f32_e32 v52, v52
	v_cvt_f32_i32_e32 v43, v43
	v_cvt_f32_i32_e32 v42, v42
	v_exp_f32_e32 v53, v53
	v_cvt_f32_i32_e32 v49, v49
	v_cvt_f32_i32_e32 v48, v48
	v_add_f32_e32 v52, 1.0, v52
	v_pk_mul_f32 v[42:43], v[138:139], v[42:43]
	v_add_f32_e32 v53, 1.0, v53
	v_add_u32_e32 v72, 0x80, v168
	v_rcp_f32_e32 v52, v52
	v_rcp_f32_e32 v53, v53
	v_pk_mul_f32 v[42:43], v[46:47], v[42:43]
	v_pk_mul_f32 v[46:47], v[144:145], v[48:49]
	v_cvt_pk_bf16_f32 v61, v50, v51
	v_mad_i64_i32 v[50:51], s[24:25], v72, s62, v[114:115]
	v_mul_f32_e32 v48, v46, v54
	v_lshl_add_u64 v[50:51], v[50:51], 0, v[110:111]
	v_exp_f32_e32 v55, v48
	global_store_dwordx4 v[50:51], v[58:61], off nt
	v_add_u32_e32 v51, 0x90, v168
	v_mul_f32_e32 v50, v219, v219
	v_pk_mul_f32 v[48:49], v[50:51], v[52:53] op_sel_hi:[0,1]
	v_pk_mul_f32 v[42:43], v[42:43], v[48:49]
	v_cvt_f32_i32_e32 v45, v45
	v_cvt_pk_bf16_f32 v42, v42, v43
	v_add_f32_e32 v43, 1.0, v55
	v_rcp_f32_e32 v48, v43
	v_mul_f32_e32 v43, v47, v54
	v_exp_f32_e32 v43, v43
	v_cvt_f32_i32_e32 v44, v44
	v_cvt_f32_i32_e32 v39, v39
	v_cvt_f32_i32_e32 v38, v38
	v_add_f32_e32 v43, 1.0, v43
	v_rcp_f32_e32 v49, v43
	v_pk_mul_f32 v[44:45], v[140:141], v[44:45]
	v_pk_mul_f32 v[38:39], v[134:135], v[38:39]
	v_pk_mul_f32 v[44:45], v[46:47], v[44:45]
	v_pk_mul_f32 v[46:47], v[50:51], v[48:49] op_sel_hi:[0,1]
	v_mul_f32_e32 v43, v38, v54
	v_pk_mul_f32 v[44:45], v[44:45], v[46:47]
	v_exp_f32_e32 v52, v43
	v_cvt_pk_bf16_f32 v43, v44, v45
	v_mul_f32_e32 v45, v39, v54
	v_exp_f32_e32 v45, v45
	v_add_f32_e32 v44, 1.0, v52
	v_cvt_f32_i32_e32 v35, v35
	v_cvt_f32_i32_e32 v34, v34
	v_add_f32_e32 v45, 1.0, v45
	v_rcp_f32_e32 v44, v44
	v_cvt_f32_i32_e32 v41, v41
	v_cvt_f32_i32_e32 v40, v40
	v_rcp_f32_e32 v45, v45
	v_pk_mul_f32 v[34:35], v[130:131], v[34:35]
	v_cvt_f32_i32_e32 v37, v37
	v_pk_mul_f32 v[40:41], v[136:137], v[40:41]
	v_pk_mul_f32 v[34:35], v[38:39], v[34:35]
	v_pk_mul_f32 v[38:39], v[50:51], v[44:45] op_sel_hi:[0,1]
	v_mul_f32_e32 v46, v40, v54
	v_pk_mul_f32 v[34:35], v[34:35], v[38:39]
	v_mul_f32_e32 v39, v41, v54
	v_exp_f32_e32 v46, v46
	v_exp_f32_e32 v39, v39
	v_cvt_f32_i32_e32 v36, v36
	v_cvt_pk_bf16_f32 v44, v34, v35
	v_add_f32_e32 v38, 1.0, v46
	v_add_f32_e32 v39, 1.0, v39
	v_rcp_f32_e32 v38, v38
	v_rcp_f32_e32 v39, v39
	v_pk_mul_f32 v[34:35], v[132:133], v[36:37]
	v_cvt_f32_i32_e32 v31, v31
	v_pk_mul_f32 v[34:35], v[40:41], v[34:35]
	v_pk_mul_f32 v[36:37], v[50:51], v[38:39] op_sel_hi:[0,1]
	v_pk_mul_f32 v[34:35], v[34:35], v[36:37]
	v_cvt_f32_i32_e32 v30, v30
	v_cvt_pk_bf16_f32 v45, v34, v35
	s_nop 0
	v_mad_i64_i32 v[36:37], s[24:25], v51, s62, v[114:115]
	v_lshl_add_u64 v[36:37], v[36:37], 0, v[110:111]
	v_pk_mul_f32 v[30:31], v[142:143], v[30:31]
	s_waitcnt lgkmcnt(0)
; __device__ __forceinline__ float fast_sigmoid(float x) { return __builtin_amdgcn_rcpf(1.0f + __expf(-x)); }
;     __device__ __forceinline__ void operator()(const f32x4 (&acc)[2][2][4][2], const Unit& u, int wr, int wc, int fr, int fq) const {
;     ...
;             for (int m = 0; m < 4; ++m) { const size_t off = (size_t)(row0 + ai * HALF + m * 16) * ldc + col0;
;                 const float rs = IN8 ? rt.tab[sl * 256 + wr * 64 + ai * HALF + m * 16 + fr] : isc;
;                 const float rsn = rs * -1.4426950408889634f, rs2 = rs * rs; (void)rsn; (void)rs2;
;                 float o[8];
; #pragma unroll
;                 for (int n = 0; n < 2; ++n)
; #pragma unroll
;                     for (int e = 0; e < 4; ++e) { const float ga = acc[ai][0][m][n][e], ua = acc[ai][1][m][n][e];
;                         if (IN8) {
;                             const float gq = (float)__float_as_int(ga) * cg[n][e], uq = (float)__float_as_int(ua) * cu[n][e];
;                             const float sg = __builtin_amdgcn_rcpf(1.0f + __builtin_amdgcn_exp2f(gq * rsn));
;                             o[4 * n + e] = (gq * uq) * (sg * rs2); }
;                         else { const float g = ga * rs, up = ua * rs; o[4 * n + e] = g * fast_sigmoid(g) * up; } }
;                 if (F8) { unsigned w0 = 0u, w1 = 0u;
; #pragma unroll
;                     for (int e = 0; e < 8; ++e) o[e] = __builtin_amdgcn_fmed3f(o[e] * H8_SCALE, -448.0f, 448.0f);
;                     w0 = __builtin_amdgcn_cvt_pk_fp8_f32(o[0], o[1], w0, false); w0 = __builtin_amdgcn_cvt_pk_fp8_f32(o[2], o[3], w0, true);
;                     w1 = __builtin_amdgcn_cvt_pk_fp8_f32(o[4], o[5], w1, false); w1 = __builtin_amdgcn_cvt_pk_fp8_f32(o[6], o[7], w1, true);
;                     typedef unsigned u32x2_ __attribute__((ext_vector_type(2))); *(u32x2_*)((unsigned char*)O + off) = (u32x2_){w0, w1}; }
;                 else { u32x4 w; w.x = cvt_pk_bf16(o[0], o[1]); w.y = cvt_pk_bf16(o[2], o[3]); w.z = cvt_pk_bf16(o[4], o[5]); w.w = cvt_pk_bf16(o[6], o[7]);
;                     __builtin_nontemporal_store(w, (u32x4*)((bf16_t*)O + off)); } }
	v_mul_f32_e32 v38, 0xbfb8aa3b, v220
	v_mul_f32_e32 v39, v30, v38
	global_store_dwordx4 v[36:37], v[42:45], off nt
	v_mul_f32_e32 v37, v31, v38
	v_exp_f32_e32 v39, v39
	v_cvt_f32_i32_e32 v27, v27
	v_cvt_f32_i32_e32 v26, v26
	v_exp_f32_e32 v37, v37
	v_cvt_f32_i32_e32 v33, v33
	v_cvt_f32_i32_e32 v32, v32
	v_add_f32_e32 v36, 1.0, v39
	v_pk_mul_f32 v[26:27], v[138:139], v[26:27]
	v_add_f32_e32 v37, 1.0, v37
	v_rcp_f32_e32 v36, v36
	v_rcp_f32_e32 v37, v37
	v_pk_mul_f32 v[26:27], v[30:31], v[26:27]
	v_pk_mul_f32 v[30:31], v[144:145], v[32:33]
	v_mul_f32_e32 v220, v220, v220
	v_mul_f32_e32 v32, v30, v38
	v_exp_f32_e32 v39, v32
	v_pk_mul_f32 v[32:33], v[220:221], v[36:37] op_sel_hi:[0,1]
	v_pk_mul_f32 v[26:27], v[26:27], v[32:33]
	v_cvt_f32_i32_e32 v29, v29
	v_cvt_pk_bf16_f32 v26, v26, v27
	v_add_f32_e32 v27, 1.0, v39
	v_rcp_f32_e32 v32, v27
	v_mul_f32_e32 v27, v31, v38
	v_exp_f32_e32 v27, v27
	v_cvt_f32_i32_e32 v28, v28
	v_cvt_f32_i32_e32 v23, v23
	v_cvt_f32_i32_e32 v22, v22
	v_add_f32_e32 v27, 1.0, v27
	v_rcp_f32_e32 v33, v27
	v_pk_mul_f32 v[28:29], v[140:141], v[28:29]
	v_pk_mul_f32 v[22:23], v[134:135], v[22:23]
	v_pk_mul_f32 v[28:29], v[30:31], v[28:29]
	v_pk_mul_f32 v[30:31], v[220:221], v[32:33] op_sel_hi:[0,1]
	v_mul_f32_e32 v27, v22, v38
	v_pk_mul_f32 v[28:29], v[28:29], v[30:31]
	v_exp_f32_e32 v36, v27
	v_cvt_pk_bf16_f32 v27, v28, v29
	v_mul_f32_e32 v29, v23, v38
	v_exp_f32_e32 v29, v29
	v_add_f32_e32 v28, 1.0, v36
	v_cvt_f32_i32_e32 v19, v19
	v_cvt_f32_i32_e32 v18, v18
	v_add_f32_e32 v29, 1.0, v29
	v_rcp_f32_e32 v28, v28
	v_cvt_f32_i32_e32 v25, v25
	v_cvt_f32_i32_e32 v24, v24
	v_rcp_f32_e32 v29, v29
	v_pk_mul_f32 v[18:19], v[130:131], v[18:19]
	v_cvt_f32_i32_e32 v21, v21
	v_pk_mul_f32 v[24:25], v[136:137], v[24:25]
	v_pk_mul_f32 v[18:19], v[22:23], v[18:19]
	v_pk_mul_f32 v[22:23], v[220:221], v[28:29] op_sel_hi:[0,1]
	v_mul_f32_e32 v30, v24, v38
	v_pk_mul_f32 v[18:19], v[18:19], v[22:23]
	v_mul_f32_e32 v23, v25, v38
	v_exp_f32_e32 v30, v30
	v_exp_f32_e32 v23, v23
	v_cvt_f32_i32_e32 v20, v20
	v_cvt_f32_i32_e32 v15, v15
	v_add_f32_e32 v22, 1.0, v30
	v_add_f32_e32 v23, 1.0, v23
	v_rcp_f32_e32 v22, v22
	v_rcp_f32_e32 v23, v23
	v_cvt_f32_i32_e32 v14, v14
	v_cvt_pk_bf16_f32 v28, v18, v19
	v_pk_mul_f32 v[18:19], v[132:133], v[20:21]
	v_pk_mul_f32 v[20:21], v[220:221], v[22:23] op_sel_hi:[0,1]
	v_pk_mul_f32 v[18:19], v[24:25], v[18:19]
	v_mul_f32_e32 v22, 0xbfb8aa3b, v221
	v_pk_mul_f32 v[14:15], v[142:143], v[14:15]
	v_pk_mul_f32 v[18:19], v[18:19], v[20:21]
	v_mul_f32_e32 v20, v14, v22
	v_mul_f32_e32 v21, v15, v22
	v_exp_f32_e32 v20, v20
	v_cvt_f32_i32_e32 v11, v11
	v_cvt_f32_i32_e32 v10, v10
	v_exp_f32_e32 v21, v21
	v_cvt_f32_i32_e32 v17, v17
	v_cvt_f32_i32_e32 v16, v16
	v_add_f32_e32 v20, 1.0, v20
	v_pk_mul_f32 v[10:11], v[138:139], v[10:11]
	v_add_f32_e32 v21, 1.0, v21
	v_add_u32_e32 v40, 0xa0, v168
	v_rcp_f32_e32 v20, v20
	v_rcp_f32_e32 v21, v21
	v_pk_mul_f32 v[10:11], v[14:15], v[10:11]
	v_pk_mul_f32 v[14:15], v[144:145], v[16:17]
	v_cvt_pk_bf16_f32 v29, v18, v19
	v_mad_i64_i32 v[18:19], s[24:25], v40, s62, v[114:115]
	v_mul_f32_e32 v16, v14, v22
	v_lshl_add_u64 v[18:19], v[18:19], 0, v[110:111]
	v_exp_f32_e32 v23, v16
	global_store_dwordx4 v[18:19], v[26:29], off nt
	v_add_u32_e32 v19, 0xb0, v168
	v_mul_f32_e32 v18, v221, v221
	v_pk_mul_f32 v[16:17], v[18:19], v[20:21] op_sel_hi:[0,1]
	v_pk_mul_f32 v[10:11], v[10:11], v[16:17]
	v_cvt_f32_i32_e32 v13, v13
	v_cvt_pk_bf16_f32 v10, v10, v11
	v_add_f32_e32 v11, 1.0, v23
	v_rcp_f32_e32 v16, v11
	v_mul_f32_e32 v11, v15, v22
	v_exp_f32_e32 v11, v11
	v_cvt_f32_i32_e32 v12, v12
	v_cvt_f32_i32_e32 v7, v7
	v_cvt_f32_i32_e32 v6, v6
	v_add_f32_e32 v11, 1.0, v11
	v_rcp_f32_e32 v17, v11
	v_pk_mul_f32 v[12:13], v[140:141], v[12:13]
	v_pk_mul_f32 v[6:7], v[134:135], v[6:7]
	v_pk_mul_f32 v[12:13], v[14:15], v[12:13]
	v_pk_mul_f32 v[14:15], v[18:19], v[16:17] op_sel_hi:[0,1]
	v_mul_f32_e32 v11, v6, v22
	v_pk_mul_f32 v[12:13], v[12:13], v[14:15]
	v_exp_f32_e32 v20, v11
	v_cvt_pk_bf16_f32 v11, v12, v13
	v_mul_f32_e32 v13, v7, v22
	v_exp_f32_e32 v13, v13
	v_add_f32_e32 v12, 1.0, v20
	v_cvt_f32_i32_e32 v3, v3
	v_cvt_f32_i32_e32 v2, v2
	v_add_f32_e32 v13, 1.0, v13
	v_rcp_f32_e32 v12, v12
	v_cvt_f32_i32_e32 v9, v9
	v_cvt_f32_i32_e32 v8, v8
	v_rcp_f32_e32 v13, v13
	v_pk_mul_f32 v[2:3], v[130:131], v[2:3]
	v_cvt_f32_i32_e32 v5, v5
	v_pk_mul_f32 v[8:9], v[136:137], v[8:9]
	v_pk_mul_f32 v[2:3], v[6:7], v[2:3]
	v_pk_mul_f32 v[6:7], v[18:19], v[12:13] op_sel_hi:[0,1]
	v_mul_f32_e32 v14, v8, v22
	v_pk_mul_f32 v[2:3], v[2:3], v[6:7]
	v_mul_f32_e32 v7, v9, v22
	v_exp_f32_e32 v14, v14
	v_exp_f32_e32 v7, v7
	v_cvt_f32_i32_e32 v4, v4
	v_cvt_pk_bf16_f32 v12, v2, v3
	v_add_f32_e32 v6, 1.0, v14
	v_add_f32_e32 v7, 1.0, v7
	v_rcp_f32_e32 v6, v6
	v_rcp_f32_e32 v7, v7
	v_pk_mul_f32 v[2:3], v[132:133], v[4:5]
	s_andn2_b64 vcc, exec, s[0:1]
	v_pk_mul_f32 v[2:3], v[8:9], v[2:3]
	v_pk_mul_f32 v[4:5], v[18:19], v[6:7] op_sel_hi:[0,1]
	v_pk_mul_f32 v[2:3], v[2:3], v[4:5]
	s_mov_b64 s[0:1], -1
	v_cvt_pk_bf16_f32 v13, v2, v3
	v_mad_i64_i32 v[2:3], s[24:25], v19, s62, v[114:115]
	v_lshl_add_u64 v[2:3], v[2:3], 0, v[110:111]
	global_store_dwordx4 v[2:3], v[10:13], off nt
	s_cbranch_vccnz .LBB0_222
	s_andn2_b64 vcc, exec, s[4:5]
	s_cbranch_vccnz .LBB0_221
	s_barrier
	s_branch .LBB0_221
